# final + FILL_E 6 instead of 8 (fewer conversion grabs beside phase E GEMM)
# speedup vs baseline: 1.0088x; 1.0088x over previous
.LBB0_1641:
	s_mul_i32 s2, s76, 0xd760
	s_add_i32 s2, s2, 0xc300
	s_sub_i32 s82, s11, s4
	s_max_i32 s57, s50, s2
	s_mul_i32 s2, s82, 0x180
	s_add_i32 s2, s2, s57
	s_min_i32 s50, s2, 0x34920
	s_cmp_lt_i32 s74, 0
	s_mov_b64 s[2:3], -1
	s_cbranch_scc0 .LBB0_2087
	s_ashr_i32 s9, s10, 6
	s_not_b32 s83, s74
	s_lshl_b32 s3, s9, 3
	s_lshl_b32 s2, s83, 6
	s_add_i32 s54, s57, s3
	s_add_i32 s42, s54, s2
	s_cmp_lt_i32 s42, s50
	s_cselect_b32 s77, s42, -1
	s_cmp_lt_i32 s77, 0
	v_and_b32_e32 v132, 63, v1
	s_cbranch_scc1 .LBB0_1654
	s_mul_hi_u32 s2, s77, 0x9824d8ed
	s_lshr_b32 s2, s2, 15
	s_mul_i32 s3, s2, 0xd760
	s_sub_i32 s24, s77, s3
	s_cmpk_gt_u32 s24, 0xc2ff
	s_mov_b64 s[20:21], -1
	s_cbranch_scc0 .LBB0_1675
	s_add_i32 s20, s2, 1
	s_add_i32 s3, s24, 0xffff3d00
	s_cmpk_lt_u32 s3, 0x1400
	s_cselect_b32 s3, s3, s24
	s_cmpk_gt_u32 s3, 0xbff
	s_mov_b64 s[22:23], -1
	s_cbranch_scc0 .LBB0_1672
	s_cmpk_gt_u32 s3, 0x13ff
	s_cbranch_scc0 .LBB0_1669
	s_add_u32 s25, s78, 0x6200000
	s_addc_u32 s26, s79, 0
	s_cmpk_gt_u32 s3, 0x93ff
	s_cbranch_scc0 .LBB0_1666
	s_add_u32 s27, s78, 0x26a00000
	s_addc_u32 s28, s79, 0
	s_cmpk_gt_u32 s3, 0xd3ff
	s_cbranch_scc0 .LBB0_1663
	s_cmpk_gt_u32 s3, 0xd5ff
	s_cbranch_scc0 .LBB0_1660
	s_cmpk_gt_u32 s3, 0xd6ff
	s_cbranch_scc0 .LBB0_1657
	s_lshl_b32 s22, s3, 5
	s_cmpk_gt_u32 s3, 0xd71f
	s_mov_b64 s[18:19], -1
	s_cbranch_scc0 .LBB0_1652
	s_mov_b32 s21, s47
	v_readlane_b32 s56, v243, 40
	s_lshl_b64 s[10:11], s[20:21], 19
	v_readlane_b32 s62, v243, 46
	v_readlane_b32 s63, v243, 47
	s_add_u32 s16, s62, s10
	s_addc_u32 s17, s63, s11
	s_lshl_b64 s[10:11], s[20:21], 18
	s_add_u32 s8, s78, s10
	s_addc_u32 s13, s79, s11
	s_add_u32 s10, s8, 0x37000000
	s_addc_u32 s11, s13, 0
	s_add_u32 s12, s8, 0x37100000
	v_readlane_b32 s58, v243, 42
	s_addc_u32 s13, s13, 0
	s_lshl_b32 s8, s20, 13
	v_readlane_b32 s59, v243, 43
	s_add_u32 s14, s58, s8
	s_addc_u32 s15, s59, 0
	s_and_b32 s8, s22, 0x7fffffc0
	v_readlane_b32 s57, v243, 41
	v_readlane_b32 s60, v243, 44
	v_readlane_b32 s61, v243, 45
	v_readlane_b32 s64, v243, 48
	v_readlane_b32 s65, v243, 49
	v_readlane_b32 s66, v243, 50
	v_readlane_b32 s67, v243, 51
	v_readlane_b32 s68, v243, 52
	v_readlane_b32 s69, v243, 53
	v_readlane_b32 s70, v243, 54
	v_readlane_b32 s71, v243, 55
	s_add_i32 s8, s8, 0xffe51c00
	s_and_b32 s89, s22, 32
	s_mov_b64 s[18:19], 0
